# maxbr + MFMA zero-init + loop-invariant LDS-DMA M0 offsets kept in SGPRs (no per-head v_readfirstlane)
# baseline (speedup 1.0000x reference)
_Z7k_fusedPKDF16_S0_S0_S0_PKfS2_S2_Pf:
	v_lshrrev_b32_e32 v222, 6, v0
	v_and_b32_e32 v1, 63, v0
	s_load_dwordx8 s[24:31], s[0:1], 0x8
	s_load_dwordx4 s[36:39], s[0:1], 0x28
	v_lshlrev_b32_e32 v4, 2, v222
	v_lshlrev_b32_e32 v5, 3, v1
	v_lshl_or_b32 v2, v222, 11, v5
	v_lshlrev_b32_e32 v224, 12, v222
	v_or_b32_e32 v6, 1, v4
	v_lshlrev_b32_e32 v223, 1, v2
	v_readfirstlane_b32 s3, v224
	v_lshl_or_b32 v2, v6, 9, v5
	v_lshlrev_b32_e32 v225, 10, v6
	v_mov_b32_e32 v211, 0
	s_mov_b32 m0, s3
	v_lshlrev_b32_e32 v210, 1, v2
	v_readfirstlane_b32 s3, v225
	s_waitcnt lgkmcnt(0)
	global_load_lds_dwordx4 v223, s[24:25]
	v_lshl_add_u64 v[2:3], s[24:25], 0, v[210:211]
	s_mov_b32 m0, s3
	v_or_b32_e32 v6, 2, v4
	global_load_lds_dwordx4 v[2:3], off
	v_lshl_or_b32 v2, v6, 9, v5
	v_lshlrev_b32_e32 v212, 1, v2
	v_mov_b32_e32 v213, v211
	v_lshl_add_u64 v[2:3], s[24:25], 0, v[212:213]
	v_lshlrev_b32_e32 v213, 10, v6
	v_or_b32_e32 v4, 3, v4
	v_readfirstlane_b32 s3, v213
	s_mov_b32 m0, s3
	v_mov_b32_e32 v215, v211
	global_load_lds_dwordx4 v[2:3], off
	v_lshl_or_b32 v2, v4, 9, v5
	v_lshlrev_b32_e32 v214, 1, v2
	v_lshl_add_u64 v[2:3], s[24:25], 0, v[214:215]
	v_lshlrev_b32_e32 v215, 10, v4
	s_nop 0
	v_readfirstlane_b32 s3, v215
	s_mov_b32 m0, s3
	s_movk_i32 s3, 0xff
	global_load_lds_dwordx4 v[2:3], off
	v_and_b32_e32 v2, 0x7f, v0
	v_lshlrev_b32_e32 v2, 2, v2
	global_load_dword v4, v2, s[36:37]
	global_load_dword v5, v2, s[38:39]
	s_lshl_b32 s3, s2, 8
	s_load_dwordx2 s[4:5], s[0:1], 0x0
	v_and_b32_e32 v6, 0xff, v0
	v_or_b32_e32 v6, s3, v6
	v_ashrrev_i32_e32 v7, 31, v6
	v_lshl_add_u64 v[6:7], v[6:7], 2, s[30:31]
	global_load_dword v244, v[6:7], off
	v_mov_b32_e32 v208, s3
	v_lshl_or_b32 v2, s2, 3, v222
	v_ashrrev_i32_e32 v3, 31, v2
	v_lshlrev_b64 v[2:3], 13, v[2:3]
	s_waitcnt lgkmcnt(0)
	v_lshl_add_u64 v[6:7], s[4:5], 0, v[2:3]
	v_mov_b32_e32 v2, 0
	v_lshlrev_b32_e32 v206, 4, v1
	v_mov_b32_e32 v207, v2
	v_lshl_add_u64 v[6:7], v[6:7], 0, v[206:207]
	v_lshlrev_b32_e32 v211, 13, v222
	v_ashrrev_i32_e32 v209, 31, v208
	v_lshl_add_u64 v[8:9], v[208:209], 2, s[30:31]
	v_or_b32_e32 v3, v211, v206
	v_lshl_add_u64 v[8:9], v[8:9], 0, v[206:207]
	global_load_dwordx4 v[68:71], v[8:9], off
	global_load_dwordx4 v[130:133], v[6:7], off
	global_load_dwordx4 v[134:137], v[6:7], off offset:1024
	global_load_dwordx4 v[138:141], v[6:7], off offset:2048
	global_load_dwordx4 v[142:145], v[6:7], off offset:3072
	s_movk_i32 s33, 0x1000
	v_add_co_u32_e32 v14, vcc, s33, v6
	s_nop 1
	v_addc_co_u32_e32 v15, vcc, 0, v7, vcc
	global_load_dwordx4 v[146:149], v[14:15], off
	global_load_dwordx4 v[150:153], v[14:15], off offset:1024
	global_load_dwordx4 v[154:157], v[14:15], off offset:2048
	global_load_dwordx4 v[158:161], v[14:15], off offset:3072
	v_lshlrev_b32_e32 v10, 1, v3
	global_load_dwordx4 v[186:189], v10, s[28:29] offset:16
	global_load_dwordx4 v[190:193], v10, s[28:29]
	global_load_dwordx4 v[178:181], v10, s[28:29] offset:2064
	global_load_dwordx4 v[182:185], v10, s[28:29] offset:2048
	v_mov_b32_e32 v11, v2
	v_lshl_add_u64 v[8:9], s[28:29], 0, v[10:11]
	v_add_co_u32_e32 v12, vcc, s33, v8
	s_mov_b64 s[34:35], 0x1000
	s_nop 0
	v_addc_co_u32_e32 v13, vcc, 0, v9, vcc
	s_mov_b64 s[40:41], 0x1800
	v_lshl_add_u64 v[10:11], v[8:9], 0, s[34:35]
	v_lshl_add_u64 v[8:9], v[8:9], 0, s[40:41]
	global_load_dwordx4 v[170:173], v[12:13], off
	global_load_dwordx4 v[174:177], v[10:11], off offset:16
	global_load_dwordx4 v[162:165], v[12:13], off offset:2048
	global_load_dwordx4 v[166:169], v[8:9], off offset:16
	s_waitcnt vmcnt(17)
	v_cmp_gt_u32_e32 vcc, 0x100, v0
	s_and_saveexec_b64 s[4:5], vcc
	v_lshlrev_b32_e32 v12, 4, v0
	v_and_b32_e32 v13, 0xe3, v0
	v_lshlrev_b32_e32 v14, 1, v0
	v_and_b32_e32 v12, 64, v12
	s_mov_b32 s8, 0x20000
	v_and_b32_e32 v14, 48, v14
	v_lshl_or_b32 v13, v13, 2, v12
	v_or3_b32 v13, v13, v14, s8
	v_add_f32_e32 v12, -1.0, v244
	v_mul_f32_e32 v12, 0x47000000, v12
	v_mul_f32_e32 v12, 0x3fb8aa3b, v12
	ds_write_b32 v13, v12
	s_or_b64 exec, exec, s[4:5]
	s_waitcnt lgkmcnt(0)
	s_barrier
	ds_read_b128 v[4:7], v206 offset:8192
	ds_read_b128 v[72:75], v206 offset:9216
	s_load_dwordx2 s[30:31], s[0:1], 0x38
	s_mov_b32 s0, 0x47000000
	s_mov_b32 s42, 0x3fb8aa3b
	s_mov_b32 s43, 0xff800000
	v_lshrrev_b32_e32 v96, 5, v1
	v_lshlrev_b32_e32 v97, 4, v96
	v_lshl_or_b32 v209, v222, 11, v206
	v_lshlrev_b32_e32 v1, 5, v1
	s_add_u32 s54, s24, 0x8000
	v_lshlrev_b32_e32 v207, 2, v96
	s_addc_u32 s55, s25, 0
	v_or_b32_e32 v227, 0x10000, v3
	s_mov_b32 s56, 0xc1d00000
	s_mov_b64 s[44:45], 0x20000
	s_mov_b64 s[46:47], 0x20800
	s_mov_b64 s[48:49], 0x21000
	s_mov_b32 s57, 0x21000
	s_mov_b64 s[50:51], 0x21800
	v_mov_b32_e32 v194, 0x3c003c00
	s_waitcnt lgkmcnt(0)
	s_waitcnt vmcnt(15)
	v_mfma_f32_32x32x16_f16 v[36:51], v[4:7], v[130:133], 0
	ds_read_b128 v[4:7], v206
	ds_read_b128 v[76:79], v206 offset:1024
	ds_read_b128 v[20:23], v206 offset:24576
	ds_read_b128 v[80:83], v206 offset:25600
	ds_read_b128 v[52:55], v206 offset:16384
	ds_read_b128 v[84:87], v206 offset:17408
	v_max_f32_e32 v71, v71, v71
	s_waitcnt lgkmcnt(1)
	v_mfma_f32_32x32x16_f16 v[52:67], v[130:133], v[52:55], 0
	v_max_f32_e32 v70, v70, v70
	v_max_f32_e32 v70, v70, v71
	s_waitcnt vmcnt(14)
	v_mfma_f32_32x32x16_f16 v[36:51], v[72:75], v[134:137], v[36:51]
	s_waitcnt lgkmcnt(0)
	v_mfma_f32_32x32x16_f16 v[52:67], v[134:137], v[84:87], v[52:67]
	ds_read_b128 v[72:75], v206 offset:10240
	ds_read_b128 v[84:87], v206 offset:11264
	s_waitcnt lgkmcnt(1)
	s_waitcnt vmcnt(13)
	v_mfma_f32_32x32x16_f16 v[36:51], v[72:75], v[138:141], v[36:51]
	ds_read_b128 v[72:75], v206 offset:18432
	ds_read_b128 v[88:91], v206 offset:19456
	s_waitcnt lgkmcnt(1)
	v_mfma_f32_32x32x16_f16 v[52:67], v[138:141], v[72:75], v[52:67]
	ds_read_b128 v[72:75], v206 offset:12288
	s_waitcnt vmcnt(12)
	v_mfma_f32_32x32x16_f16 v[36:51], v[84:87], v[142:145], v[36:51]
	v_mbcnt_lo_u32_b32 v84, -1, 0
	v_mbcnt_hi_u32_b32 v92, -1, v84
	ds_read_b128 v[84:87], v206 offset:13312
	v_xor_b32_e32 v93, 1, v92
	v_xor_b32_e32 v94, 2, v92
	v_xor_b32_e32 v95, 4, v92
	s_waitcnt lgkmcnt(2)
	v_mfma_f32_32x32x16_f16 v[52:67], v[142:145], v[88:91], v[52:67]
	v_and_b32_e32 v88, 64, v92
	v_add_u32_e32 v98, 64, v88
	v_cmp_lt_i32_e32 vcc, v93, v98
	ds_read_b128 v[88:91], v206 offset:21504
	s_waitcnt lgkmcnt(2)
	s_waitcnt vmcnt(11)
	v_mfma_f32_32x32x16_f16 v[36:51], v[72:75], v[146:149], v[36:51]
	ds_read_b128 v[72:75], v206 offset:20480
	s_waitcnt lgkmcnt(0)
	v_mfma_f32_32x32x16_f16 v[52:67], v[146:149], v[72:75], v[52:67]
	v_cndmask_b32_e32 v72, v92, v93, vcc
	v_lshlrev_b32_e32 v72, 2, v72
	v_max3_f32 v73, v68, v69, v70
	ds_bpermute_b32 v72, v72, v73
	v_cmp_lt_i32_e32 vcc, v94, v98
	s_waitcnt lgkmcnt(0)
	v_max_f32_e32 v72, v72, v72
	v_cndmask_b32_e32 v68, v92, v94, vcc
	v_lshlrev_b32_e32 v74, 2, v68
	ds_read_b128 v[68:71], v206 offset:14336
	s_waitcnt vmcnt(10)
	v_mfma_f32_32x32x16_f16 v[36:51], v[84:87], v[150:153], v[36:51]
	v_max_f32_e32 v84, v73, v72
	ds_bpermute_b32 v85, v74, v84
	v_cmp_lt_i32_e32 vcc, v95, v98
	s_waitcnt lgkmcnt(0)
	v_max_f32_e32 v85, v85, v85
	v_mfma_f32_32x32x16_f16 v[52:67], v[150:153], v[88:91], v[52:67]
	v_cndmask_b32_e32 v72, v92, v95, vcc
	v_lshlrev_b32_e32 v86, 2, v72
	v_max_f32_e32 v92, v84, v85
	ds_read_b128 v[72:75], v206 offset:15360
	ds_bpermute_b32 v93, v86, v92
	s_waitcnt lgkmcnt(0)
	v_max_f32_e32 v93, v93, v93
	s_waitcnt vmcnt(9)
	v_mfma_f32_32x32x16_f16 v[36:51], v[68:71], v[154:157], v[36:51]
	ds_read_b128 v[68:71], v206 offset:22528
	ds_read_b128 v[84:87], v206 offset:23552
	v_max_f32_e32 v92, v92, v93
	global_load_dwordx4 v[88:91], v97, s[36:37]
	v_readlane_b32 s3, v92, 0
	v_readlane_b32 s2, v92, 8
	v_readlane_b32 s5, v92, 16
	v_readlane_b32 s4, v92, 24
	s_waitcnt lgkmcnt(1)
	v_mfma_f32_32x32x16_f16 v[52:67], v[154:157], v[68:71], v[52:67]
	v_add_f32_e64 v68, s2, -1.0
	v_add_f32_e64 v69, s3, -1.0
	v_readlane_b32 s7, v92, 32
	v_readlane_b32 s6, v92, 40
	v_add_f32_e64 v70, s4, -1.0
	v_add_f32_e64 v71, s5, -1.0
	v_pk_mul_f32 v[68:69], v[68:69], s[0:1] op_sel_hi:[1,0]
	v_readlane_b32 s9, v92, 48
	v_readlane_b32 s8, v92, 56
	v_mfma_f32_32x32x16_f16 v[20:35], v[20:23], v[130:133], 0
	v_mul_f32_e64 v70, v70, s0
	v_mul_f32_e64 v71, v71, s0
	v_mul_f32_e64 v92, v68, s42
	v_mul_f32_e64 v93, v69, s42
	v_mul_f32_e64 v94, v70, s42
	v_mul_f32_e64 v95, v71, s42
	v_max3_f32 v68, v93, s43, v92
	v_max3_f32 v68, v68, v95, v94
	s_waitcnt vmcnt(9)
	v_mfma_f32_32x32x16_f16 v[36:51], v[72:75], v[158:161], v[36:51]
	v_add_f32_e64 v72, s6, -1.0
	v_add_f32_e64 v73, s7, -1.0
	v_mul_f32_e64 v72, v72, s0
	v_mul_f32_e64 v73, v73, s0
	s_waitcnt lgkmcnt(0)
	v_mfma_f32_32x32x16_f16 v[52:67], v[158:161], v[84:87], v[52:67]
	v_mul_f32_e64 v84, v72, s42
	v_mul_f32_e64 v85, v73, s42
	v_add_f32_e64 v86, s8, -1.0
	v_add_f32_e64 v87, s9, -1.0
	v_max3_f32 v98, v68, v85, v84
	ds_read_b128 v[68:71], v206 offset:26624
	v_cvt_pk_f16_f32 v43, v42, v43
	v_cvt_pk_f16_f32 v42, v40, v41
	v_cvt_pk_f16_f32 v41, v38, v39
	v_mfma_f32_32x32x16_f16 v[20:35], v[80:83], v[134:137], v[20:35]
	v_mul_f32_e64 v80, v86, s0
	v_mul_f32_e64 v81, v87, s0
	v_cvt_pk_f16_f32 v40, v36, v37
	v_mul_f32_e64 v86, v80, s42
	v_mul_f32_e64 v87, v81, s42
	global_load_dwordx4 v[72:75], v97, s[36:37] offset:32
	v_max3_f32 v80, v98, v87, v86
	v_add_f32_e32 v98, 0xc53b8000, v80
	ds_read_b128 v[80:83], v206 offset:27648
	global_load_dwordx4 v[36:39], v97, s[36:37] offset:64
	ds_write_b128 v209, v[40:43] offset:32768
	v_cvt_pk_f16_f32 v43, v50, v51
	v_cvt_pk_f16_f32 v40, v44, v45
	v_cvt_pk_f16_f32 v44, v52, v53
	global_load_dwordx4 v[50:53], v97, s[36:37] offset:96
	s_waitcnt lgkmcnt(2)
	v_mfma_f32_32x32x16_f16 v[20:35], v[68:71], v[138:141], v[20:35]
	ds_read_b128 v[68:71], v206 offset:28672
	v_cvt_pk_f16_f32 v42, v48, v49
	v_cvt_pk_f16_f32 v41, v46, v47
	ds_write_b128 v209, v[40:43] offset:33792
	ds_read_b128 v[40:43], v206 offset:30720
	v_cvt_pk_f16_f32 v47, v58, v59
	v_cvt_pk_f16_f32 v46, v56, v57
	s_waitcnt lgkmcnt(4)
	v_mfma_f32_32x32x16_f16 v[20:35], v[80:83], v[142:145], v[20:35]
	ds_read_b128 v[80:83], v206 offset:29696
	v_cvt_pk_f16_f32 v45, v54, v55
	ds_write_b128 v209, v[44:47] offset:49152
	v_cvt_pk_f16_f32 v45, v66, v67
	ds_read_b128 v[46:49], v206 offset:31744
	v_cvt_pk_f16_f32 v44, v64, v65
	v_cmp_ge_f32_e64 s[0:1], v92, v98
	s_waitcnt lgkmcnt(5)
	v_mfma_f32_32x32x16_f16 v[20:35], v[68:71], v[146:149], v[20:35]
	v_cmp_ge_f32_e64 s[2:3], v93, v98
	v_cmp_ge_f32_e64 s[4:5], v94, v98
	v_cmp_ge_f32_e64 s[6:7], v95, v98
	v_cmp_ge_f32_e64 s[8:9], v84, v98
	v_cmp_ge_f32_e64 s[10:11], v85, v98
	v_cmp_ge_f32_e64 s[12:13], v86, v98
	v_cmp_ge_f32_e64 s[14:15], v87, v98
	v_mfma_f32_32x32x16_f16 v[4:19], v[4:7], v[130:133], 0
	s_waitcnt lgkmcnt(2)
	v_mfma_f32_32x32x16_f16 v[20:35], v[80:83], v[150:153], v[20:35]
	v_mfma_f32_32x32x16_f16 v[4:19], v[76:79], v[134:137], v[4:19]
	v_mfma_f32_32x32x16_f16 v[20:35], v[40:43], v[154:157], v[20:35]
	v_cvt_pk_f16_f32 v43, v62, v63
	v_cvt_pk_f16_f32 v42, v60, v61
	ds_write_b128 v209, v[42:45] offset:50176
	ds_read_b128 v[40:43], v206 offset:2048
	ds_read_b128 v[54:57], v206 offset:3072
	s_waitcnt lgkmcnt(1)
	v_mfma_f32_32x32x16_f16 v[4:19], v[40:43], v[138:141], v[4:19]
	s_waitcnt lgkmcnt(0)
	v_mfma_f32_32x32x16_f16 v[4:19], v[54:57], v[142:145], v[4:19]
	v_mfma_f32_32x32x16_f16 v[20:35], v[46:49], v[158:161], v[20:35]
	ds_read_b128 v[44:47], v206 offset:4096
	ds_read_b128 v[58:61], v206 offset:5120
	ds_read_b128 v[62:65], v206 offset:6144
	ds_read_b128 v[66:69], v206 offset:7168
	s_waitcnt lgkmcnt(0)
	s_barrier
	s_waitcnt vmcnt(3)
	s_nop 4
	v_add_f32_e32 v20, v20, v88
	v_mfma_f32_32x32x16_f16 v[4:19], v[44:47], v[146:149], v[4:19]
	v_add_f32_e32 v21, v89, v21
	v_add_f32_e32 v22, v90, v22
	v_add_f32_e32 v23, v91, v23
	s_waitcnt vmcnt(2)
	v_add_f32_e32 v24, v24, v72
	v_add_f32_e32 v25, v73, v25
	v_add_f32_e32 v26, v74, v26
	v_add_f32_e32 v27, v75, v27
	v_mfma_f32_32x32x16_f16 v[4:19], v[58:61], v[150:153], v[4:19]
	s_waitcnt vmcnt(1)
	v_add_f32_e32 v28, v28, v36
	v_add_f32_e32 v29, v37, v29
	v_add_f32_e32 v30, v38, v30
	v_add_f32_e32 v31, v39, v31
	s_waitcnt vmcnt(0)
	v_add_f32_e32 v32, v32, v50
	v_add_f32_e32 v33, v51, v33
	v_add_f32_e32 v34, v52, v34
	v_mfma_f32_32x32x16_f16 v[4:19], v[62:65], v[154:157], v[4:19]
	v_add_f32_e32 v35, v53, v35
	v_mul_f32_e32 v20, 0xbfb8aa3b, v20
	v_mul_f32_e32 v21, 0xbfb8aa3b, v21
	v_mul_f32_e32 v22, 0xbfb8aa3b, v22
	v_mul_f32_e32 v23, 0xbfb8aa3b, v23
	v_mul_f32_e32 v24, 0xbfb8aa3b, v24
	v_mul_f32_e32 v25, 0xbfb8aa3b, v25
	v_mfma_f32_32x32x16_f16 v[4:19], v[66:69], v[158:161], v[4:19]
	v_mul_f32_e32 v26, 0xbfb8aa3b, v26
	v_mul_f32_e32 v27, 0xbfb8aa3b, v27
	v_mul_f32_e32 v28, 0xbfb8aa3b, v28
	v_mul_f32_e32 v29, 0xbfb8aa3b, v29
	v_mul_f32_e32 v30, 0xbfb8aa3b, v30
	v_mul_f32_e32 v31, 0xbfb8aa3b, v31
	v_mul_f32_e32 v32, 0xbfb8aa3b, v32
	v_mul_f32_e32 v33, 0xbfb8aa3b, v33
	v_mul_f32_e32 v34, 0xbfb8aa3b, v34
	v_mul_f32_e32 v35, 0xbfb8aa3b, v35
	v_exp_f32_e32 v20, v20
	v_exp_f32_e32 v21, v21
	v_exp_f32_e32 v22, v22
	v_exp_f32_e32 v23, v23
	v_exp_f32_e32 v24, v24
	v_exp_f32_e32 v25, v25
	v_exp_f32_e32 v26, v26
	v_exp_f32_e32 v27, v27
	v_exp_f32_e32 v28, v28
	v_exp_f32_e32 v29, v29
	v_exp_f32_e32 v30, v30
	v_exp_f32_e32 v31, v31
	v_exp_f32_e32 v32, v32
	v_exp_f32_e32 v33, v33
	v_exp_f32_e32 v34, v34
	v_exp_f32_e32 v35, v35
	v_add_f32_e32 v20, 1.0, v20
	v_add_f32_e32 v21, 1.0, v21
	v_add_f32_e32 v22, 1.0, v22
	v_add_f32_e32 v23, 1.0, v23
	v_add_f32_e32 v24, 1.0, v24
	v_add_f32_e32 v25, 1.0, v25
	v_add_f32_e32 v26, 1.0, v26
	v_add_f32_e32 v27, 1.0, v27
	v_add_f32_e32 v28, 1.0, v28
	v_add_f32_e32 v29, 1.0, v29
	v_add_f32_e32 v30, 1.0, v30
	v_add_f32_e32 v31, 1.0, v31
	v_add_f32_e32 v32, 1.0, v32
	v_add_f32_e32 v33, 1.0, v33
	v_add_f32_e32 v34, 1.0, v34
	v_add_f32_e32 v35, 1.0, v35
	v_rcp_f32_e32 v20, v20
	v_rcp_f32_e32 v21, v21
	v_rcp_f32_e32 v22, v22
	v_rcp_f32_e32 v23, v23
	v_rcp_f32_e32 v24, v24
	v_rcp_f32_e32 v25, v25
	v_rcp_f32_e32 v26, v26
	v_rcp_f32_e32 v27, v27
	v_rcp_f32_e32 v28, v28
	v_rcp_f32_e32 v29, v29
	v_rcp_f32_e32 v30, v30
	v_rcp_f32_e32 v31, v31
	v_rcp_f32_e32 v32, v32
	v_rcp_f32_e32 v33, v33
	v_rcp_f32_e32 v34, v34
	v_rcp_f32_e32 v35, v35
	v_cvt_pk_f16_f32 v198, v4, v5
	v_lshl_or_b32 v4, v222, 14, v1
	v_mov_b32_e32 v5, v2
	v_lshl_add_u64 v[216:217], s[28:29], 0, v[4:5]
	v_or_b32_e32 v4, 0x2000, v4
	v_lshrrev_b32_e32 v1, 1, v0
	v_lshl_add_u64 v[218:219], s[28:29], 0, v[4:5]
	v_and_b32_e32 v4, 16, v1
	v_mov_b32_e32 v36, 0x20000
	v_lshl_add_u64 v[4:5], s[36:37], 0, v[4:5]
	s_mov_b64 s[28:29], 0x80
	v_lshl_or_b32 v226, v96, 6, v36
	v_cvt_pk_f16_f32 v199, v6, v7
	v_cvt_pk_f16_f32 v200, v8, v9
	v_cvt_pk_f16_f32 v201, v10, v11
	v_cvt_pk_f16_f32 v202, v12, v13
	v_cvt_pk_f16_f32 v203, v14, v15
	v_cvt_pk_f16_f32 v204, v16, v17
	v_cvt_pk_f16_f32 v205, v18, v19
	v_cvt_pk_f16_f32 v229, v20, v21
	v_cvt_pk_f16_f32 v230, v22, v23
	v_cvt_pk_f16_f32 v232, v24, v25
	v_cvt_pk_f16_f32 v234, v26, v27
	v_cvt_pk_f16_f32 v228, v28, v29
	v_cvt_pk_f16_f32 v231, v30, v31
	v_cvt_pk_f16_f32 v233, v32, v33
	v_cvt_pk_f16_f32 v235, v34, v35
	v_lshl_add_u64 v[220:221], v[4:5], 0, s[28:29]
	s_mov_b64 s[36:37], 0
	v_readfirstlane_b32 s78, v224
	s_nop 3
	s_add_u32 s79, s78, 0x400
	s_add_u32 s80, s78, 0x800
	s_add_u32 s81, s78, 0xc00
	s_branch .LBB1_6

.Ltri1_done:
	s_cmp_lg_u32 s36, 0x60000
	s_cselect_b64 s[52:53], -1, 0
	s_cmp_eq_u32 s36, 0x60000
	s_cselect_b32 s23, s27, s55
	s_cselect_b32 s22, s26, s54
	s_setprio 0
	s_mov_b32 m0, s78
	s_nop 0
	global_load_lds_dwordx4 v223, s[22:23]
	s_mov_b32 m0, s79
	s_nop 0
	global_load_lds_dwordx4 v210, s[22:23]
	s_mov_b32 m0, s80
	s_nop 0
	global_load_lds_dwordx4 v212, s[22:23]
	s_mov_b32 m0, s81
	s_nop 0
	global_load_lds_dwordx4 v214, s[22:23]
	v_mov_b32_e32 v243, 0xff800000
	s_not_b64 s[22:23], s[2:3]
	s_andn2_b64 vcc, exec, s[2:3]
	v_mov_b32_e32 v1, 0xff800000
	s_cbranch_vccz .LBB1_64
